# baseline (speedup 1.0000x reference)
_Z8k3_chainPKfPK15HIP_vector_typeIiLj4EEPKtS6_S0_S0_Pf:
	s_load_dwordx8 s[8:15], s[0:1], 0x0
	s_load_dwordx4 s[4:7], s[0:1], 0x20
	s_load_dwordx2 s[16:17], s[0:1], 0x30
	s_mul_hi_u32 s0, s2, 0xaaaaaaab
	s_lshr_b32 s20, s0, 5
	s_mul_i32 s0, s20, 48
	s_mov_b32 s21, 0
	s_sub_i32 s18, s2, s0
	s_lshl_b64 s[0:1], s[20:21], 13
	s_waitcnt lgkmcnt(0)
	s_add_u32 s2, s10, s0
	v_and_b32_e32 v1, 3, v0
	s_addc_u32 s3, s11, s1
	s_mul_hi_u32 s1, s20, 0x18000
	s_mul_i32 s0, s20, 0x18000
	v_lshlrev_b32_e32 v104, 4, v0
	v_mov_b32_e32 v105, 0
	v_lshl_or_b32 v98, s18, 2, v1
	s_lshl_b64 s[18:19], s[0:1], 4
	v_lshl_add_u64 v[2:3], s[2:3], 0, v[104:105]
	s_add_u32 s0, s8, s18
	s_movk_i32 s8, 0x1000
	v_add_co_u32_e32 v10, vcc, s8, v2
	s_addc_u32 s1, s9, s19
	s_nop 0
	v_addc_co_u32_e32 v11, vcc, 0, v3, vcc
	global_load_dwordx4 v[2:5], v104, s[2:3]
	global_load_dwordx4 v[6:9], v[10:11], off
	s_mul_i32 s2, s20, 0x6000
	s_mul_hi_u32 s3, s20, 0x6000
	s_add_u32 s2, s12, s2
	s_addc_u32 s3, s13, s3
	v_lshl_add_u64 v[10:11], s[2:3], 0, v[104:105]
	v_lshrrev_b32_e32 v124, 6, v0
	s_movk_i32 s8, 0x2000
	v_add_co_u32_e32 v12, vcc, s8, v10
	s_movk_i32 s8, 0x3000
	s_nop 0
	v_addc_co_u32_e32 v13, vcc, 0, v11, vcc
	v_readfirstlane_b32 s36, v124
	s_lshl_b32 s36, s36, 10
	s_add_u32 s36, s36, 0x8040
	s_mov_b32 m0, s36
	s_mov_b64 s[38:39], 0x1000
	global_load_lds_dwordx4 v[10:11], off
	s_add_u32 s37, s36, 0x1000
	s_mov_b32 m0, s37
	v_lshl_add_u64 v[126:127], v[10:11], 0, s[38:39]
	s_add_u32 s37, s36, 0x2000
	global_load_lds_dwordx4 v[126:127], off
	s_mov_b32 m0, s37
	s_add_u32 s37, s36, 0x3000
	global_load_lds_dwordx4 v[12:13], off
	v_add_co_u32_e32 v12, vcc, s8, v10
	v_lshrrev_b32_e32 v110, 2, v0
	s_nop 0
	v_addc_co_u32_e32 v13, vcc, 0, v11, vcc
	v_or_b32_e32 v14, 0x4000, v104
	s_mov_b32 m0, s37
	s_add_u32 s37, s36, 0x4000
	global_load_lds_dwordx4 v[12:13], off
	s_mov_b32 m0, s37
	s_add_u32 s37, s36, 0x5000
	global_load_lds_dwordx4 v14, s[2:3]
	s_movk_i32 s2, 0x5000
	v_add_co_u32_e32 v10, vcc, s2, v10
	s_movk_i32 s2, 0xc0
	v_or_b32_e32 v18, 64, v110
	v_addc_co_u32_e32 v11, vcc, 0, v11, vcc
	v_mov_b32_e32 v99, v105
	v_mad_u32_u24 v106, v110, s2, v98
	v_mov_b32_e32 v107, v105
	v_mul_u32_u24_e32 v102, 0xc00, v18
	v_mov_b32_e32 v103, v105
	s_mov_b32 m0, s37
	s_nop 0
	global_load_lds_dwordx4 v[10:11], off
	v_lshlrev_b64 v[10:11], 4, v[106:107]
	v_lshl_add_u64 v[14:15], s[0:1], 0, v[102:103]
	v_lshlrev_b64 v[16:17], 4, v[98:99]
	v_lshl_add_u64 v[12:13], s[0:1], 0, v[10:11]
	v_lshl_add_u64 v[14:15], v[14:15], 0, v[16:17]
	s_mov_b32 s3, 0x30000
	global_load_dwordx4 v[58:61], v[12:13], off
	global_load_dwordx4 v[62:65], v[14:15], off
	v_add_co_u32_e32 v12, vcc, s3, v14
	s_mov_b32 s3, 0x60000
	s_nop 0
	v_addc_co_u32_e32 v13, vcc, 0, v15, vcc
	v_add_co_u32_e32 v14, vcc, s3, v14
	s_movk_i32 s2, 0xc00
	s_nop 0
	v_addc_co_u32_e32 v15, vcc, 0, v15, vcc
	global_load_dwordx4 v[70:73], v[12:13], off
	global_load_dwordx4 v[74:77], v[14:15], off
	v_mov_b32_e32 v12, 0x90000
	v_mad_u32_u24 v12, v18, s2, v12
	v_mov_b32_e32 v13, v105
	v_mov_b32_e32 v14, 0xc0000
	v_lshl_add_u64 v[12:13], s[0:1], 0, v[12:13]
	v_mad_u32_u24 v100, v18, s2, v14
	v_mov_b32_e32 v101, v105
	v_lshl_add_u64 v[12:13], v[12:13], 0, v[16:17]
	v_lshl_add_u64 v[14:15], s[0:1], 0, v[100:101]
	v_lshl_add_u64 v[14:15], v[14:15], 0, v[16:17]
	global_load_dwordx4 v[78:81], v[12:13], off
	global_load_dwordx4 v[82:85], v[14:15], off
	v_mov_b32_e32 v12, 0xf0000
	v_mad_u32_u24 v96, v18, s2, v12
	v_mov_b32_e32 v97, v105
	v_mov_b32_e32 v14, 0x120000
	v_lshl_add_u64 v[12:13], s[0:1], 0, v[96:97]
	v_mad_u32_u24 v94, v18, s2, v14
	v_mov_b32_e32 v95, v105
	v_lshl_add_u64 v[12:13], v[12:13], 0, v[16:17]
	v_lshl_add_u64 v[14:15], s[0:1], 0, v[94:95]
	v_lshl_add_u64 v[14:15], v[14:15], 0, v[16:17]
	global_load_dwordx4 v[86:89], v[12:13], off
	global_load_dwordx4 v[90:93], v[14:15], off
	s_waitcnt vmcnt(15)
	ds_write_b128 v104, v[2:5] offset:57408
	s_waitcnt vmcnt(14)
	ds_write_b128 v104, v[6:9] offset:61504
	v_lshl_add_u64 v[2:3], s[6:7], 0, v[10:11]
	s_waitcnt lgkmcnt(0)
	s_barrier
	global_load_dwordx4 v[34:37], v[2:3], off
	v_lshl_add_u64 v[2:3], s[4:5], 0, v[10:11]
	v_add_u32_e32 v4, 0x3000, v106
	v_mov_b32_e32 v5, v105
	v_lshl_add_u64 v[4:5], v[4:5], 4, s[4:5]
	global_load_dwordx4 v[30:33], v[2:3], off
	global_load_dwordx4 v[26:29], v[4:5], off
	v_add_u32_e32 v2, 0x6000, v106
	v_mov_b32_e32 v3, v105
	v_lshl_add_u64 v[2:3], v[2:3], 4, s[4:5]
	v_add_u32_e32 v4, 0x9000, v106
	v_mov_b32_e32 v5, v105
	v_lshl_add_u64 v[4:5], v[4:5], 4, s[4:5]
	global_load_dwordx4 v[22:25], v[2:3], off
	global_load_dwordx4 v[18:21], v[4:5], off
	v_add_u32_e32 v2, 0xc000, v106
	v_mov_b32_e32 v3, v105
	v_lshl_add_u64 v[2:3], v[2:3], 4, s[4:5]
	v_add_u32_e32 v4, 0xf000, v106
	v_mov_b32_e32 v5, v105
	v_lshl_add_u64 v[4:5], v[4:5], 4, s[4:5]
	global_load_dwordx4 v[14:17], v[2:3], off
	global_load_dwordx4 v[10:13], v[4:5], off
	v_add_u32_e32 v2, 0x12000, v106
	v_mov_b32_e32 v3, v105
	v_lshl_add_u64 v[108:109], v[2:3], 4, s[4:5]
	v_add_u32_e32 v2, 0x15000, v106
	v_lshl_add_u64 v[106:107], v[2:3], 4, s[4:5]
	global_load_dwordx4 v[6:9], v[108:109], off
	global_load_dwordx4 v[2:5], v[106:107], off
	v_bfe_u32 v113, v0, 5, 1
	v_lshrrev_b32_e32 v115, 6, v0
	v_lshlrev_b32_e32 v112, 2, v113
	v_and_b32_e32 v111, 31, v0
	v_or_b32_e32 v116, v112, v115
	v_lshl_or_b32 v120, v116, 5, v111
	v_lshlrev_b32_e32 v108, 4, v120
	ds_read_b32 v140, v108 offset:57420
	ds_read_b32 v141, v108 offset:61516
	ds_read_u16 v158, v108 offset:57408
	ds_read_u16 v159, v108 offset:61504
	v_lshlrev_b32_e32 v142, 9, v116
	v_add_u32_e32 v142, 0x200, v142
	v_add_u32_e32 v143, 0x1000, v142
	v_mov_b32_e32 v152, 0x2000
	s_waitcnt lgkmcnt(0)
	v_cmp_lt_u32_e64 s[28:29], 12, v158
	v_cmp_lt_u32_e64 s[30:31], 12, v159
	v_ffbl_b32_e32 v153, v140
	v_ffbl_b32_e32 v154, v141
	v_cmp_ne_u32_e32 vcc, 0, v140
	v_cmp_ne_u32_e64 s[22:23], 0, v141
	v_lshl_add_u32 v153, v153, 4, v142
	v_lshl_add_u32 v154, v154, 4, v143
	v_cndmask_b32_e32 v144, v152, v153, vcc
	v_cndmask_b32_e64 v160, v152, v154, s[22:23]
	v_add_u32_e32 v153, -1, v140
	v_add_u32_e32 v154, -1, v141
	v_and_b32_e32 v140, v153, v140
	v_and_b32_e32 v141, v154, v141
	v_ffbl_b32_e32 v153, v140
	v_ffbl_b32_e32 v154, v141
	v_cmp_ne_u32_e32 vcc, 0, v140
	v_cmp_ne_u32_e64 s[22:23], 0, v141
	v_lshl_add_u32 v153, v153, 4, v142
	v_lshl_add_u32 v154, v154, 4, v143
	v_cndmask_b32_e32 v145, v152, v153, vcc
	v_cndmask_b32_e64 v161, v152, v154, s[22:23]
	v_add_u32_e32 v153, -1, v140
	v_add_u32_e32 v154, -1, v141
	v_and_b32_e32 v140, v153, v140
	v_and_b32_e32 v141, v154, v141
	v_ffbl_b32_e32 v153, v140
	v_ffbl_b32_e32 v154, v141
	v_cmp_ne_u32_e32 vcc, 0, v140
	v_cmp_ne_u32_e64 s[22:23], 0, v141
	v_lshl_add_u32 v153, v153, 4, v142
	v_lshl_add_u32 v154, v154, 4, v143
	v_cndmask_b32_e32 v146, v152, v153, vcc
	v_cndmask_b32_e64 v162, v152, v154, s[22:23]
	v_add_u32_e32 v153, -1, v140
	v_add_u32_e32 v154, -1, v141
	v_and_b32_e32 v140, v153, v140
	v_and_b32_e32 v141, v154, v141
	v_ffbl_b32_e32 v153, v140
	v_ffbl_b32_e32 v154, v141
	v_cmp_ne_u32_e32 vcc, 0, v140
	v_cmp_ne_u32_e64 s[22:23], 0, v141
	v_lshl_add_u32 v153, v153, 4, v142
	v_lshl_add_u32 v154, v154, 4, v143
	v_cndmask_b32_e32 v147, v152, v153, vcc
	v_cndmask_b32_e64 v163, v152, v154, s[22:23]
	v_add_u32_e32 v153, -1, v140
	v_add_u32_e32 v154, -1, v141
	v_and_b32_e32 v140, v153, v140
	v_and_b32_e32 v141, v154, v141
	v_ffbl_b32_e32 v153, v140
	v_ffbl_b32_e32 v154, v141
	v_cmp_ne_u32_e32 vcc, 0, v140
	v_cmp_ne_u32_e64 s[22:23], 0, v141
	v_lshl_add_u32 v153, v153, 4, v142
	v_lshl_add_u32 v154, v154, 4, v143
	v_cndmask_b32_e32 v148, v152, v153, vcc
	v_cndmask_b32_e64 v164, v152, v154, s[22:23]
	v_add_u32_e32 v153, -1, v140
	v_add_u32_e32 v154, -1, v141
	v_and_b32_e32 v140, v153, v140
	v_and_b32_e32 v141, v154, v141
	v_lshl_or_b32 v144, v145, 16, v144
	v_lshl_or_b32 v145, v147, 16, v146
	v_lshl_or_b32 v146, v158, 16, v148
	v_mov_b32_e32 v147, v140
	v_lshl_or_b32 v160, v161, 16, v160
	v_lshl_or_b32 v161, v163, 16, v162
	v_lshl_or_b32 v162, v159, 16, v164
	v_mov_b32_e32 v163, v141
	v_add_u32_e32 v153, 0x118c0, v108
	ds_write_b128 v153, v[144:147]
	ds_write_b128 v153, v[160:163] offset:4096
	ds_read_b64 v[106:107], v108 offset:57408
	ds_read_u16 v118, v108 offset:57410
	v_and_b32_e32 v114, 63, v0
	v_and_b32_e32 v0, 32, v0
	v_add_u32_e32 v117, 0xe040, v108
	v_mov_b32_e32 v108, -1
	v_mov_b32_e32 v119, v105
	s_branch .LBB2_2

.LBB2_12:
	s_or_b64 exec, exec, s[12:13]
	v_lshlrev_b32_e32 v106, 9, v119
	v_ffbl_b32_e32 v107, v107
	v_ffbl_b32_e32 v108, v108
	v_lshlrev_b32_e32 v116, 25, v119
	v_lshl_or_b32 v107, v107, 4, v106
	v_mov_b32_e32 v109, 0x2000
	v_lshl_or_b32 v108, v108, 20, v116
	v_bfrev_b32_e32 v116, 4
	v_ffbl_b32_e32 v0, v0
	v_cndmask_b32_e64 v107, v107, v109, s[8:9]
	v_cndmask_b32_e64 v108, v108, v116, s[4:5]
	v_lshl_or_b32 v0, v0, 4, v106
	v_cndmask_b32_e32 v0, v0, v109, vcc
	v_or_b32_e32 v106, v108, v107
	v_mov_b32_e32 v108, 0x800000
	v_lshlrev_b32_e32 v107, 16, v117
	v_cndmask_b32_e64 v108, 0, v108, s[6:7]
	s_waitcnt lgkmcnt(2)
	v_lshl_or_b32 v0, v118, 24, v0
	v_or3_b32 v0, v0, v108, v107
	ds_write2_b32 v105, v106, v0 offset0:1 offset1:3
	v_cmp_ne_u32_e32 vcc, 0, v140
	v_cmp_ne_u32_e64 s[22:23], 0, v141
	v_lshlrev_b32_e32 v150, 5, v113
	v_lshl_add_u32 v155, v113, 2, v115
	v_lshlrev_b32_e32 v155, 2, v155
	v_add_u32_e32 v155, 0x11840, v155
	v_lshrrev_b64 v[146:147], v150, vcc
	v_lshrrev_b64 v[156:157], v150, s[22:23]
	v_mov_b32_e32 v151, 0x400
	v_cmp_ne_u32_e32 vcc, 0, v146
	v_cmp_ne_u32_e64 s[22:23], 0, v156
	s_nop 1
	v_cndmask_b32_e32 v146, 0, v151, vcc
	v_cndmask_b32_e64 v156, 0, v151, s[22:23]
	v_lshrrev_b64 v[148:149], v150, s[28:29]
	v_lshrrev_b64 v[152:153], v150, s[30:31]
	v_mov_b32_e32 v154, 0x800
	v_cmp_ne_u32_e32 vcc, 0, v148
	v_cmp_ne_u32_e64 s[22:23], 0, v152
	s_nop 1
	v_cndmask_b32_e32 v148, 0, v154, vcc
	v_cndmask_b32_e64 v152, 0, v154, s[22:23]
	v_or_b32_e32 v146, v146, v148
	v_or_b32_e32 v156, v156, v152
	v_lshl_add_u32 v148, v113, 2, v115
	v_lshl_or_b32 v148, v148, 5, v111
	v_lshlrev_b32_e32 v149, 2, v148
	v_add_u32_e32 v149, 0x11040, v149
	v_lshlrev_b32_e32 v148, 4, v148
	ds_read_b32 v152, v149
	ds_read_b32 v153, v149 offset:1024
	s_waitcnt lgkmcnt(0)
	ds_write_b32 v148, v152 offset:57408
	ds_write_b32 v148, v153 offset:61504
	v_cmp_eq_u32_e32 vcc, 0, v111
	s_and_saveexec_b64 s[22:23], vcc
	ds_or_b32 v155, v146
	ds_or_b32 v155, v156 offset:32
	s_or_b64 exec, exec, s[22:23]
	s_movk_i32 s2, 0x2010
	v_mul_u32_u24_e32 v105, 0x2010, v115
	v_cmp_eq_u32_e32 vcc, 0, v114
	s_and_saveexec_b64 s[0:1], vcc
	v_mov_b32_e32 v38, 0
	v_mov_b32_e32 v39, v38
	v_mov_b32_e32 v40, v38
	v_mov_b32_e32 v41, v38
	ds_write_b128 v105, v[38:41] offset:8192
	s_or_b64 exec, exec, s[0:1]
	v_lshlrev_b32_e32 v40, 3, v113
	v_lshlrev_b32_e32 v67, 4, v110
	v_or_b32_e32 v38, 0x1e0, v111
	v_or_b32_e32 v0, 0x8040, v40
	v_mad_u32_u24 v66, v1, s2, v67
	v_mad_u32_u24 v38, v38, 48, v0
	s_waitcnt vmcnt(16)
	ds_write_b128 v66, v[58:61]
	s_waitcnt vmcnt(15)
	ds_write_b128 v66, v[62:65] offset:1024
	s_waitcnt vmcnt(14)
	ds_write_b128 v66, v[70:73] offset:2048
	s_waitcnt vmcnt(13)
	ds_write_b128 v66, v[74:77] offset:3072
	s_waitcnt vmcnt(12)
	ds_write_b128 v66, v[78:81] offset:4096
	s_waitcnt vmcnt(11)
	ds_write_b128 v66, v[82:85] offset:5120
	s_waitcnt vmcnt(10)
	ds_write_b128 v66, v[86:89] offset:6144
	s_waitcnt vmcnt(9)
	ds_write_b128 v66, v[90:93] offset:7168
	v_lshl_add_u32 v116, v113, 3, v105
	v_or_b32_e32 v106, 0x1e0, v111
	v_lshlrev_b32_e32 v138, 4, v106
	v_add_u32_e32 v139, 0x118c0, v138
	v_mul_u32_u24_e32 v156, 48, v106
	v_add_u32_e32 v156, v0, v156
	v_mov_b32_e32 v157, 0x1187c
	v_add_u32_e32 v137, v116, v138
	v_add_u32_e32 v138, 0x200, v138
	v_lshlrev_b32_e32 v160, 4, v111
	v_lshlrev_b32_e32 v161, 3, v111
	v_add_u32_e32 v161, 0x118c0, v161
	v_mul_u32_u24_e32 v162, 48, v111
	v_add_u32_e32 v162, v0, v162
	v_mov_b32_e32 v163, 0x11840
	v_mul_hi_u32_u24_e32 v159, 0x410, v111
	v_mul_u32_u24_e32 v158, 0x410, v111
	v_mov_b32_e32 v107, 0x82000
	v_mad_u64_u32 v[158:159], s[0:1], s20, v107, v[158:159]
	v_lshlrev_b32_e32 v107, 3, v113
	v_or_b32_e32 v158, v158, v107
	v_lshl_add_u64 v[158:159], s[14:15], 0, v[158:159]
	s_mov_b64 s[0:1], 0x79e30
	s_mov_b32 s2, 0xffff7e00
	s_mov_b32 s3, -1
	v_lshl_add_u64 v[158:159], v[158:159], 0, s[0:1]
	v_lshl_add_u32 v107, v114, 2, v163
	v_add_u32_e32 v107, -8, v107
	s_waitcnt lgkmcnt(0)
	s_barrier
	ds_read_b128 v[38:41], v138 offset:56896
	ds_read_b128 v[42:45], v139
	ds_read2_b64 v[56:59], v156 offset1:2
	ds_read_b32 v60, v107
	v_add_u32_e32 v156, 0xfffffa00, v156
	ds_read2_b64 v[52:55], v156 offset1:2
	v_add_u32_e32 v106, -2, v114
	v_cmp_gt_u32_e32 vcc, 16, v106
	s_waitcnt lgkmcnt(0)
	v_cndmask_b32_e32 v60, 0, v60, vcc
	s_nop 1
	v_readlane_b32 s4, v60, 17
	v_readlane_b32 s21, v60, 16
	v_add_u32_sdwa v92, v105, v56 dst_sel:DWORD dst_unused:UNUSED_PAD src0_sel:DWORD src1_sel:WORD_0
	v_add_u32_sdwa v93, v105, v56 dst_sel:DWORD dst_unused:UNUSED_PAD src0_sel:DWORD src1_sel:WORD_1
	v_add_u32_sdwa v106, v105, v57 dst_sel:DWORD dst_unused:UNUSED_PAD src0_sel:DWORD src1_sel:WORD_0
	v_add_u32_sdwa v107, v105, v57 dst_sel:DWORD dst_unused:UNUSED_PAD src0_sel:DWORD src1_sel:WORD_1
	v_add_u32_sdwa v108, v105, v58 dst_sel:DWORD dst_unused:UNUSED_PAD src0_sel:DWORD src1_sel:WORD_0
	v_add_u32_sdwa v109, v105, v58 dst_sel:DWORD dst_unused:UNUSED_PAD src0_sel:DWORD src1_sel:WORD_1
	ds_read_b128 v[120:123], v92
	ds_read_b128 v[124:127], v93
	ds_read_b128 v[128:131], v106
	ds_read_b128 v[132:135], v107
	ds_read_b128 v[140:143], v108
	ds_read_b128 v[144:147], v109
	v_add_u32_sdwa v88, v116, v42 dst_sel:DWORD dst_unused:UNUSED_PAD src0_sel:DWORD src1_sel:WORD_0
	v_add_u32_sdwa v89, v116, v42 dst_sel:DWORD dst_unused:UNUSED_PAD src0_sel:DWORD src1_sel:WORD_1
	v_add_u32_sdwa v90, v116, v43 dst_sel:DWORD dst_unused:UNUSED_PAD src0_sel:DWORD src1_sel:WORD_0
	v_add_u32_sdwa v91, v116, v43 dst_sel:DWORD dst_unused:UNUSED_PAD src0_sel:DWORD src1_sel:WORD_1
	v_add_u32_sdwa v173, v116, v44 dst_sel:DWORD dst_unused:UNUSED_PAD src0_sel:DWORD src1_sel:WORD_0
	v_bfe_u32 v117, v41, 16, 7
	v_add_u32_sdwa v118, v116, v39 dst_sel:DWORD dst_unused:UNUSED_PAD src0_sel:DWORD src1_sel:WORD_0
	v_add_u32_sdwa v119, v116, v39 dst_sel:DWORD dst_unused:UNUSED_PAD src0_sel:DWORD src1_sel:WORD_1
	v_add_u32_sdwa v136, v116, v41 dst_sel:DWORD dst_unused:UNUSED_PAD src0_sel:DWORD src1_sel:WORD_0
	s_and_b32 s9, s4, 0xff
	s_waitcnt lgkmcnt(0)
	v_pk_add_f32 v[120:121], v[120:121], v[124:125]
	v_pk_add_f32 v[122:123], v[122:123], v[126:127]
	v_pk_add_f32 v[128:129], v[128:129], v[132:133]
	v_pk_add_f32 v[130:131], v[130:131], v[134:135]
	v_pk_add_f32 v[140:141], v[140:141], v[144:145]
	v_pk_add_f32 v[142:143], v[142:143], v[146:147]
	s_and_b32 s24, s4, 0x900
	s_cbranch_scc1 .Lfarx_pre
